# fast GQA attention loop v3: all softmax VALU, K/V staging and next-tile row max placed between MFMAs; permlane32 swap replaces LDS bpermute
# speedup vs baseline: 1.0908x; 1.0071x over previous
.Lfa_entry:
	s_mov_b32 s29, 0
	s_mov_b32 s40, 1
	s_add_i32 s41, s23, 0xfffff000
	s_movk_i32 s10, 0x6a00
	v_add3_u32 v217, v201, v202, s10
	v_add_u32_e32 v216, v210, v208
	v_add_u32_e32 v218, v211, v200
	v_add_u32_e32 v208, 9216, v218
	v_add_u32_e32 v210, 13568, v218
	v_add_u32_e32 v200, 27136, v218
	v_add_u32_e32 v211, 31488, v218
	s_nop 7
	s_nop 7
	v_max3_f32 v214, v48, v64, v49
	v_max3_f32 v214, v214, v65, v50
	v_max3_f32 v214, v214, v66, v51
	v_max3_f32 v214, v214, v67, v52
	v_max3_f32 v214, v214, v68, v53
	v_max3_f32 v214, v214, v69, v54
	v_max3_f32 v214, v214, v70, v55
	v_max3_f32 v214, v214, v71, v56
	v_max3_f32 v214, v214, v72, v57
	v_max3_f32 v214, v214, v73, v58
	v_max3_f32 v214, v214, v74, v59
	v_max3_f32 v214, v214, v75, v60
	v_max3_f32 v214, v214, v76, v61
	v_max3_f32 v214, v214, v77, v62
	v_max3_f32 v214, v214, v78, v63
	v_max_f32_e32 v214, v214, v79
	v_mov_b32_e32 v218, v214
	s_nop 1
	v_permlane32_swap_b32_e32 v214, v218
	v_max_f32_e32 v214, v214, v218
.Lfa_loop:
	ds_read_b128 v[112:115], v216 offset:17920
	ds_read_b128 v[116:119], v216 offset:22528
	ds_read_b128 v[120:123], v216 offset:17952
	ds_read_b128 v[124:127], v216 offset:22560
	ds_read2_b64 v[128:131], v208 offset1:2
	ds_read2_b64 v[132:135], v210 offset1:2
	ds_read2_b64 v[136:139], v208 offset0:4 offset1:6
	ds_read2_b64 v[140:143], v210 offset0:4 offset1:6
	s_cmp_lg_u32 s40, 0
	s_cbranch_scc1 .Lfa_resc0
	v_cmp_lt_f32_e32 vcc, 0x40c00000, v214
	s_cbranch_vccnz .Lfa_resc0
.Lfa_cont0:
	v_exp_f32_e32 v48, v48
	v_exp_f32_e32 v49, v49
	v_exp_f32_e32 v50, v50
	v_exp_f32_e32 v51, v51
	s_waitcnt lgkmcnt(7)
	v_mfma_f32_32x32x16_bf16 v[80:95], v[112:115], v[144:147], v[32:47]
	v_exp_f32_e32 v52, v52
	v_exp_f32_e32 v53, v53
	v_exp_f32_e32 v54, v54
	v_exp_f32_e32 v55, v55
	s_waitcnt lgkmcnt(6)
	v_mfma_f32_32x32x16_bf16 v[96:111], v[116:119], v[144:147], v[32:47]
	v_add_f32_e32 v213, v48, v49
	v_add_f32_e32 v213, v213, v50
	v_add_f32_e32 v213, v213, v51
	s_waitcnt lgkmcnt(5)
	v_mfma_f32_32x32x16_bf16 v[80:95], v[120:123], v[148:151], v[80:95]
	v_add_f32_e32 v213, v213, v52
	v_add_f32_e32 v213, v213, v53
	v_add_f32_e32 v213, v213, v54
	v_add_f32_e32 v213, v213, v55
	s_waitcnt lgkmcnt(4)
	v_mfma_f32_32x32x16_bf16 v[96:111], v[124:127], v[148:151], v[96:111]
	v_cvt_pk_bf16_f32 v48, v48, v49
	v_cvt_pk_bf16_f32 v49, v50, v51
	v_cvt_pk_bf16_f32 v50, v52, v53
	v_cvt_pk_bf16_f32 v51, v54, v55
	ds_read_b128 v[112:115], v216 offset:17984
	ds_read_b128 v[116:119], v216 offset:22592
	ds_read_b128 v[120:123], v216 offset:18016
	ds_read_b128 v[124:127], v216 offset:22624
	v_exp_f32_e32 v56, v56
	v_exp_f32_e32 v57, v57
	s_waitcnt lgkmcnt(7)
	v_mfma_f32_32x32x16_bf16 v[0:15], v[128:131], v[48:51], v[0:15]
	v_exp_f32_e32 v58, v58
	v_exp_f32_e32 v59, v59
	v_exp_f32_e32 v60, v60
	s_waitcnt lgkmcnt(6)
	v_mfma_f32_32x32x16_bf16 v[16:31], v[132:135], v[48:51], v[16:31]
	v_exp_f32_e32 v61, v61
	v_exp_f32_e32 v62, v62
	v_exp_f32_e32 v63, v63
	s_waitcnt lgkmcnt(3)
	v_mfma_f32_32x32x16_bf16 v[80:95], v[112:115], v[152:155], v[80:95]
	v_add_f32_e32 v213, v213, v56
	v_add_f32_e32 v213, v213, v57
	v_add_f32_e32 v213, v213, v58
	v_add_f32_e32 v213, v213, v59
	s_waitcnt lgkmcnt(2)
	v_mfma_f32_32x32x16_bf16 v[96:111], v[116:119], v[152:155], v[96:111]
	v_add_f32_e32 v213, v213, v60
	v_add_f32_e32 v213, v213, v61
	v_add_f32_e32 v213, v213, v62
	v_add_f32_e32 v213, v213, v63
	v_cvt_pk_bf16_f32 v56, v56, v57
	v_cvt_pk_bf16_f32 v57, v58, v59
	v_cvt_pk_bf16_f32 v58, v60, v61
	v_cvt_pk_bf16_f32 v59, v62, v63
	v_exp_f32_e32 v64, v64
	v_exp_f32_e32 v65, v65
	v_mfma_f32_32x32x16_bf16 v[0:15], v[136:139], v[56:59], v[0:15]
	v_exp_f32_e32 v66, v66
	v_exp_f32_e32 v67, v67
	v_exp_f32_e32 v68, v68
	v_mfma_f32_32x32x16_bf16 v[16:31], v[140:143], v[56:59], v[16:31]
	ds_read2_b64 v[128:131], v208 offset0:8 offset1:10
	ds_read2_b64 v[132:135], v210 offset0:8 offset1:10
	ds_read2_b64 v[136:139], v208 offset0:12 offset1:14
	ds_read2_b64 v[140:143], v210 offset0:12 offset1:14
	v_exp_f32_e32 v69, v69
	v_exp_f32_e32 v70, v70
	v_exp_f32_e32 v71, v71
	s_waitcnt lgkmcnt(5)
	v_mfma_f32_32x32x16_bf16 v[80:95], v[120:123], v[156:159], v[80:95]
	v_add_f32_e32 v213, v213, v64
	v_add_f32_e32 v213, v213, v65
	v_add_f32_e32 v213, v213, v66
	v_add_f32_e32 v213, v213, v67
	s_waitcnt lgkmcnt(4)
	v_mfma_f32_32x32x16_bf16 v[96:111], v[124:127], v[156:159], v[96:111]
	v_add_f32_e32 v213, v213, v68
	v_add_f32_e32 v213, v213, v69
	v_add_f32_e32 v213, v213, v70
	v_add_f32_e32 v213, v213, v71
	v_cvt_pk_bf16_f32 v64, v64, v65
	v_cvt_pk_bf16_f32 v65, v66, v67
	v_cvt_pk_bf16_f32 v66, v68, v69
	v_cvt_pk_bf16_f32 v67, v70, v71
	v_exp_f32_e32 v72, v72
	v_exp_f32_e32 v73, v73
	s_waitcnt lgkmcnt(3)
	v_mfma_f32_32x32x16_bf16 v[0:15], v[128:131], v[64:67], v[0:15]
	v_exp_f32_e32 v74, v74
	v_exp_f32_e32 v75, v75
	v_exp_f32_e32 v76, v76
	s_waitcnt lgkmcnt(2)
	v_mfma_f32_32x32x16_bf16 v[16:31], v[132:135], v[64:67], v[16:31]
	v_exp_f32_e32 v77, v77
	v_exp_f32_e32 v78, v78
	v_exp_f32_e32 v79, v79
	s_add_i32 s10, s29, 6
	s_min_i32 s10, s10, 0x43
	s_cmp_lt_i32 s10, 64
	s_cselect_b32 s11, s20, s41
	s_lshl_b32 s10, s10, 6
	s_add_i32 s10, s10, s11
	v_add_u32_e32 v112, s10, v197
	s_movk_i32 s10, 0x4a00
	v_mad_i64_i32 v[112:113], s[10:11], v112, s10, v[204:205]
	s_add_i32 s14, s29, 5
	s_min_i32 s14, s14, 0x43
	s_lshl_b32 s14, s14, 6
	s_mov_b32 s15, 0
	v_add_f32_e32 v213, v213, v72
	v_add_f32_e32 v213, v213, v73
	v_add_f32_e32 v213, v213, v74
	v_add_f32_e32 v213, v213, v75
	s_waitcnt vmcnt(7)
	ds_write_b128 v199, v[164:167]
	s_waitcnt vmcnt(6)
	ds_write2_b64 v217, v[160:161], v[162:163] offset1:1
	v_lshl_add_u64 v[114:115], s[14:15], 1, v[206:207]
	global_load_dwordx4 v[164:167], v[112:113], off
	global_load_dwordx4 v[160:163], v[114:115], off
	v_add_f32_e32 v213, v213, v76
	v_add_f32_e32 v213, v213, v77
	v_add_f32_e32 v213, v213, v78
	v_add_f32_e32 v213, v213, v79
	v_cvt_pk_bf16_f32 v72, v72, v73
	v_cvt_pk_bf16_f32 v73, v74, v75
	v_cvt_pk_bf16_f32 v74, v76, v77
	v_cvt_pk_bf16_f32 v75, v78, v79
	v_max3_f32 v214, v80, v96, v81
	v_max3_f32 v214, v214, v97, v82
	v_max3_f32 v214, v214, v98, v83
	v_max3_f32 v214, v214, v99, v84
	v_max3_f32 v214, v214, v100, v85
	v_max3_f32 v214, v214, v101, v86
	v_max3_f32 v214, v214, v102, v87
	v_max3_f32 v214, v214, v103, v88
	v_add_f32_e32 v212, v212, v213
	s_waitcnt lgkmcnt(3)
	v_mfma_f32_32x32x16_bf16 v[0:15], v[136:139], v[72:75], v[0:15]
	v_max3_f32 v214, v214, v104, v89
	v_max3_f32 v214, v214, v105, v90
	v_max3_f32 v214, v214, v106, v91
	v_max3_f32 v214, v214, v107, v92
	s_waitcnt lgkmcnt(2)
	v_mfma_f32_32x32x16_bf16 v[16:31], v[140:143], v[72:75], v[16:31]
	v_max3_f32 v214, v214, v108, v93
	v_max3_f32 v214, v214, v109, v94
	v_max3_f32 v214, v214, v110, v95
	v_max_f32_e32 v214, v214, v111
	v_mov_b32_e32 v218, v214
	s_nop 1
	v_permlane32_swap_b32_e32 v214, v218
	v_max_f32_e32 v214, v214, v218
	s_waitcnt lgkmcnt(0)
	s_barrier
	ds_read_b128 v[112:115], v216
	ds_read_b128 v[116:119], v216 offset:4608
	ds_read_b128 v[120:123], v216 offset:32
	ds_read_b128 v[124:127], v216 offset:4640
	ds_read2_b64 v[128:131], v200 offset1:2
	ds_read2_b64 v[132:135], v211 offset1:2
	ds_read2_b64 v[136:139], v200 offset0:4 offset1:6
	ds_read2_b64 v[140:143], v211 offset0:4 offset1:6
	s_cmp_lg_u32 s40, 0
	s_cbranch_scc1 .Lfa_resc1
	v_cmp_lt_f32_e32 vcc, 0x40c00000, v214
	s_cbranch_vccnz .Lfa_resc1
.Lfa_cont1:
	v_exp_f32_e32 v80, v80
	v_exp_f32_e32 v81, v81
	v_exp_f32_e32 v82, v82
	v_exp_f32_e32 v83, v83
	s_waitcnt lgkmcnt(7)
	v_mfma_f32_32x32x16_bf16 v[48:63], v[112:115], v[144:147], v[32:47]
	v_exp_f32_e32 v84, v84
	v_exp_f32_e32 v85, v85
	v_exp_f32_e32 v86, v86
	v_exp_f32_e32 v87, v87
	s_waitcnt lgkmcnt(6)
	v_mfma_f32_32x32x16_bf16 v[64:79], v[116:119], v[144:147], v[32:47]
	v_add_f32_e32 v213, v80, v81
	v_add_f32_e32 v213, v213, v82
	v_add_f32_e32 v213, v213, v83
	s_waitcnt lgkmcnt(5)
	v_mfma_f32_32x32x16_bf16 v[48:63], v[120:123], v[148:151], v[48:63]
	v_add_f32_e32 v213, v213, v84
	v_add_f32_e32 v213, v213, v85
	v_add_f32_e32 v213, v213, v86
	v_add_f32_e32 v213, v213, v87
	s_waitcnt lgkmcnt(4)
	v_mfma_f32_32x32x16_bf16 v[64:79], v[124:127], v[148:151], v[64:79]
	v_cvt_pk_bf16_f32 v80, v80, v81
	v_cvt_pk_bf16_f32 v81, v82, v83
	v_cvt_pk_bf16_f32 v82, v84, v85
	v_cvt_pk_bf16_f32 v83, v86, v87
	ds_read_b128 v[112:115], v216 offset:64
	ds_read_b128 v[116:119], v216 offset:4672
	ds_read_b128 v[120:123], v216 offset:96
	ds_read_b128 v[124:127], v216 offset:4704
	v_exp_f32_e32 v88, v88
	v_exp_f32_e32 v89, v89
	s_waitcnt lgkmcnt(7)
	v_mfma_f32_32x32x16_bf16 v[0:15], v[128:131], v[80:83], v[0:15]
	v_exp_f32_e32 v90, v90
	v_exp_f32_e32 v91, v91
	v_exp_f32_e32 v92, v92
	s_waitcnt lgkmcnt(6)
	v_mfma_f32_32x32x16_bf16 v[16:31], v[132:135], v[80:83], v[16:31]
	v_exp_f32_e32 v93, v93
	v_exp_f32_e32 v94, v94
	v_exp_f32_e32 v95, v95
	s_waitcnt lgkmcnt(3)
	v_mfma_f32_32x32x16_bf16 v[48:63], v[112:115], v[152:155], v[48:63]
	v_add_f32_e32 v213, v213, v88
	v_add_f32_e32 v213, v213, v89
	v_add_f32_e32 v213, v213, v90
	v_add_f32_e32 v213, v213, v91
	s_waitcnt lgkmcnt(2)
	v_mfma_f32_32x32x16_bf16 v[64:79], v[116:119], v[152:155], v[64:79]
	v_add_f32_e32 v213, v213, v92
	v_add_f32_e32 v213, v213, v93
	v_add_f32_e32 v213, v213, v94
	v_add_f32_e32 v213, v213, v95
	v_cvt_pk_bf16_f32 v88, v88, v89
	v_cvt_pk_bf16_f32 v89, v90, v91
	v_cvt_pk_bf16_f32 v90, v92, v93
	v_cvt_pk_bf16_f32 v91, v94, v95
	v_exp_f32_e32 v96, v96
	v_exp_f32_e32 v97, v97
	v_mfma_f32_32x32x16_bf16 v[0:15], v[136:139], v[88:91], v[0:15]
	v_exp_f32_e32 v98, v98
	v_exp_f32_e32 v99, v99
	v_exp_f32_e32 v100, v100
	v_mfma_f32_32x32x16_bf16 v[16:31], v[140:143], v[88:91], v[16:31]
	ds_read2_b64 v[128:131], v200 offset0:8 offset1:10
	ds_read2_b64 v[132:135], v211 offset0:8 offset1:10
	ds_read2_b64 v[136:139], v200 offset0:12 offset1:14
	ds_read2_b64 v[140:143], v211 offset0:12 offset1:14
	v_exp_f32_e32 v101, v101
	v_exp_f32_e32 v102, v102
	v_exp_f32_e32 v103, v103
	s_waitcnt lgkmcnt(5)
	v_mfma_f32_32x32x16_bf16 v[48:63], v[120:123], v[156:159], v[48:63]
	v_add_f32_e32 v213, v213, v96
	v_add_f32_e32 v213, v213, v97
	v_add_f32_e32 v213, v213, v98
	v_add_f32_e32 v213, v213, v99
	s_waitcnt lgkmcnt(4)
	v_mfma_f32_32x32x16_bf16 v[64:79], v[124:127], v[156:159], v[64:79]
	v_add_f32_e32 v213, v213, v100
	v_add_f32_e32 v213, v213, v101
	v_add_f32_e32 v213, v213, v102
	v_add_f32_e32 v213, v213, v103
	v_cvt_pk_bf16_f32 v96, v96, v97
	v_cvt_pk_bf16_f32 v97, v98, v99
	v_cvt_pk_bf16_f32 v98, v100, v101
	v_cvt_pk_bf16_f32 v99, v102, v103
	v_exp_f32_e32 v104, v104
	v_exp_f32_e32 v105, v105
	s_waitcnt lgkmcnt(3)
	v_mfma_f32_32x32x16_bf16 v[0:15], v[128:131], v[96:99], v[0:15]
	v_exp_f32_e32 v106, v106
	v_exp_f32_e32 v107, v107
	v_exp_f32_e32 v108, v108
	s_waitcnt lgkmcnt(2)
	v_mfma_f32_32x32x16_bf16 v[16:31], v[132:135], v[96:99], v[16:31]
	v_exp_f32_e32 v109, v109
	v_exp_f32_e32 v110, v110
	v_exp_f32_e32 v111, v111
	s_add_i32 s10, s29, 7
	s_min_i32 s10, s10, 0x43
	s_cmp_lt_i32 s10, 64
	s_cselect_b32 s11, s20, s41
	s_lshl_b32 s10, s10, 6
	s_add_i32 s10, s10, s11
	v_add_u32_e32 v112, s10, v197
	s_movk_i32 s10, 0x4a00
	v_mad_i64_i32 v[112:113], s[10:11], v112, s10, v[204:205]
	s_add_i32 s14, s29, 6
	s_min_i32 s14, s14, 0x43
	s_lshl_b32 s14, s14, 6
	s_mov_b32 s15, 0
	v_add_f32_e32 v213, v213, v104
	v_add_f32_e32 v213, v213, v105
	v_add_f32_e32 v213, v213, v106
	v_add_f32_e32 v213, v213, v107
	s_waitcnt vmcnt(7)
	ds_write_b128 v199, v[168:171] offset:17920
	s_waitcnt vmcnt(6)
	ds_write2_b64 v203, v[172:173], v[174:175] offset1:1
	v_lshl_add_u64 v[114:115], s[14:15], 1, v[206:207]
	global_load_dwordx4 v[168:171], v[112:113], off
	global_load_dwordx4 v[172:175], v[114:115], off
	v_add_f32_e32 v213, v213, v108
	v_add_f32_e32 v213, v213, v109
	v_add_f32_e32 v213, v213, v110
	v_add_f32_e32 v213, v213, v111
	v_cvt_pk_bf16_f32 v104, v104, v105
	v_cvt_pk_bf16_f32 v105, v106, v107
	v_cvt_pk_bf16_f32 v106, v108, v109
	v_cvt_pk_bf16_f32 v107, v110, v111
	v_max3_f32 v214, v48, v64, v49
	v_max3_f32 v214, v214, v65, v50
	v_max3_f32 v214, v214, v66, v51
	v_max3_f32 v214, v214, v67, v52
	v_max3_f32 v214, v214, v68, v53
	v_max3_f32 v214, v214, v69, v54
	v_max3_f32 v214, v214, v70, v55
	v_max3_f32 v214, v214, v71, v56
	v_add_f32_e32 v212, v212, v213
	s_waitcnt lgkmcnt(3)
	v_mfma_f32_32x32x16_bf16 v[0:15], v[136:139], v[104:107], v[0:15]
	v_max3_f32 v214, v214, v72, v57
	v_max3_f32 v214, v214, v73, v58
	v_max3_f32 v214, v214, v74, v59
	v_max3_f32 v214, v214, v75, v60
	s_waitcnt lgkmcnt(2)
	v_mfma_f32_32x32x16_bf16 v[16:31], v[140:143], v[104:107], v[16:31]
	v_max3_f32 v214, v214, v76, v61
	v_max3_f32 v214, v214, v77, v62
	v_max3_f32 v214, v214, v78, v63
	v_max_f32_e32 v214, v214, v79
	v_mov_b32_e32 v218, v214
	s_nop 1
	v_permlane32_swap_b32_e32 v214, v218
	v_max_f32_e32 v214, v214, v218
	s_waitcnt lgkmcnt(0)
	s_barrier
	ds_read_b128 v[112:115], v216 offset:17920
	ds_read_b128 v[116:119], v216 offset:22528
	ds_read_b128 v[120:123], v216 offset:17952
	ds_read_b128 v[124:127], v216 offset:22560
	ds_read2_b64 v[128:131], v208 offset1:2
	ds_read2_b64 v[132:135], v210 offset1:2
	ds_read2_b64 v[136:139], v208 offset0:4 offset1:6
	ds_read2_b64 v[140:143], v210 offset0:4 offset1:6
	s_cmp_lg_u32 s40, 0
	s_cbranch_scc1 .Lfa_resc2
	v_cmp_lt_f32_e32 vcc, 0x40c00000, v214
	s_cbranch_vccnz .Lfa_resc2
.Lfa_cont2:
	v_exp_f32_e32 v48, v48
	v_exp_f32_e32 v49, v49
	v_exp_f32_e32 v50, v50
	v_exp_f32_e32 v51, v51
	s_waitcnt lgkmcnt(7)
	v_mfma_f32_32x32x16_bf16 v[80:95], v[112:115], v[144:147], v[32:47]
	v_exp_f32_e32 v52, v52
	v_exp_f32_e32 v53, v53
	v_exp_f32_e32 v54, v54
	v_exp_f32_e32 v55, v55
	s_waitcnt lgkmcnt(6)
	v_mfma_f32_32x32x16_bf16 v[96:111], v[116:119], v[144:147], v[32:47]
	v_add_f32_e32 v213, v48, v49
	v_add_f32_e32 v213, v213, v50
	v_add_f32_e32 v213, v213, v51
	s_waitcnt lgkmcnt(5)
	v_mfma_f32_32x32x16_bf16 v[80:95], v[120:123], v[148:151], v[80:95]
	v_add_f32_e32 v213, v213, v52
	v_add_f32_e32 v213, v213, v53
	v_add_f32_e32 v213, v213, v54
	v_add_f32_e32 v213, v213, v55
	s_waitcnt lgkmcnt(4)
	v_mfma_f32_32x32x16_bf16 v[96:111], v[124:127], v[148:151], v[96:111]
	v_cvt_pk_bf16_f32 v48, v48, v49
	v_cvt_pk_bf16_f32 v49, v50, v51
	v_cvt_pk_bf16_f32 v50, v52, v53
	v_cvt_pk_bf16_f32 v51, v54, v55
	ds_read_b128 v[112:115], v216 offset:17984
	ds_read_b128 v[116:119], v216 offset:22592
	ds_read_b128 v[120:123], v216 offset:18016
	ds_read_b128 v[124:127], v216 offset:22624
	v_exp_f32_e32 v56, v56
	v_exp_f32_e32 v57, v57
	s_waitcnt lgkmcnt(7)
	v_mfma_f32_32x32x16_bf16 v[0:15], v[128:131], v[48:51], v[0:15]
	v_exp_f32_e32 v58, v58
	v_exp_f32_e32 v59, v59
	v_exp_f32_e32 v60, v60
	s_waitcnt lgkmcnt(6)
	v_mfma_f32_32x32x16_bf16 v[16:31], v[132:135], v[48:51], v[16:31]
	v_exp_f32_e32 v61, v61
	v_exp_f32_e32 v62, v62
	v_exp_f32_e32 v63, v63
	s_waitcnt lgkmcnt(3)
	v_mfma_f32_32x32x16_bf16 v[80:95], v[112:115], v[152:155], v[80:95]
	v_add_f32_e32 v213, v213, v56
	v_add_f32_e32 v213, v213, v57
	v_add_f32_e32 v213, v213, v58
	v_add_f32_e32 v213, v213, v59
	s_waitcnt lgkmcnt(2)
	v_mfma_f32_32x32x16_bf16 v[96:111], v[116:119], v[152:155], v[96:111]
	v_add_f32_e32 v213, v213, v60
	v_add_f32_e32 v213, v213, v61
	v_add_f32_e32 v213, v213, v62
	v_add_f32_e32 v213, v213, v63
	v_cvt_pk_bf16_f32 v56, v56, v57
	v_cvt_pk_bf16_f32 v57, v58, v59
	v_cvt_pk_bf16_f32 v58, v60, v61
	v_cvt_pk_bf16_f32 v59, v62, v63
	v_exp_f32_e32 v64, v64
	v_exp_f32_e32 v65, v65
	v_mfma_f32_32x32x16_bf16 v[0:15], v[136:139], v[56:59], v[0:15]
	v_exp_f32_e32 v66, v66
	v_exp_f32_e32 v67, v67
	v_exp_f32_e32 v68, v68
	v_mfma_f32_32x32x16_bf16 v[16:31], v[140:143], v[56:59], v[16:31]
	ds_read2_b64 v[128:131], v208 offset0:8 offset1:10
	ds_read2_b64 v[132:135], v210 offset0:8 offset1:10
	ds_read2_b64 v[136:139], v208 offset0:12 offset1:14
	ds_read2_b64 v[140:143], v210 offset0:12 offset1:14
	v_exp_f32_e32 v69, v69
	v_exp_f32_e32 v70, v70
	v_exp_f32_e32 v71, v71
	s_waitcnt lgkmcnt(5)
	v_mfma_f32_32x32x16_bf16 v[80:95], v[120:123], v[156:159], v[80:95]
	v_add_f32_e32 v213, v213, v64
	v_add_f32_e32 v213, v213, v65
	v_add_f32_e32 v213, v213, v66
	v_add_f32_e32 v213, v213, v67
	s_waitcnt lgkmcnt(4)
	v_mfma_f32_32x32x16_bf16 v[96:111], v[124:127], v[156:159], v[96:111]
	v_add_f32_e32 v213, v213, v68
	v_add_f32_e32 v213, v213, v69
	v_add_f32_e32 v213, v213, v70
	v_add_f32_e32 v213, v213, v71
	v_cvt_pk_bf16_f32 v64, v64, v65
	v_cvt_pk_bf16_f32 v65, v66, v67
	v_cvt_pk_bf16_f32 v66, v68, v69
	v_cvt_pk_bf16_f32 v67, v70, v71
	v_exp_f32_e32 v72, v72
	v_exp_f32_e32 v73, v73
	s_waitcnt lgkmcnt(3)
	v_mfma_f32_32x32x16_bf16 v[0:15], v[128:131], v[64:67], v[0:15]
	v_exp_f32_e32 v74, v74
	v_exp_f32_e32 v75, v75
	v_exp_f32_e32 v76, v76
	s_waitcnt lgkmcnt(2)
	v_mfma_f32_32x32x16_bf16 v[16:31], v[132:135], v[64:67], v[16:31]
	v_exp_f32_e32 v77, v77
	v_exp_f32_e32 v78, v78
	v_exp_f32_e32 v79, v79
	s_add_i32 s10, s29, 8
	s_min_i32 s10, s10, 0x43
	s_cmp_lt_i32 s10, 64
	s_cselect_b32 s11, s20, s41
	s_lshl_b32 s10, s10, 6
	s_add_i32 s10, s10, s11
	v_add_u32_e32 v112, s10, v197
	s_movk_i32 s10, 0x4a00
	v_mad_i64_i32 v[112:113], s[10:11], v112, s10, v[204:205]
	s_add_i32 s14, s29, 7
	s_min_i32 s14, s14, 0x43
	s_lshl_b32 s14, s14, 6
	s_mov_b32 s15, 0
	v_add_f32_e32 v213, v213, v72
	v_add_f32_e32 v213, v213, v73
	v_add_f32_e32 v213, v213, v74
	v_add_f32_e32 v213, v213, v75
	s_waitcnt vmcnt(7)
	ds_write_b128 v199, v[176:179]
	s_waitcnt vmcnt(6)
	ds_write2_b64 v217, v[180:181], v[182:183] offset1:1
	v_lshl_add_u64 v[114:115], s[14:15], 1, v[206:207]
	global_load_dwordx4 v[176:179], v[112:113], off
	global_load_dwordx4 v[180:183], v[114:115], off
	v_add_f32_e32 v213, v213, v76
	v_add_f32_e32 v213, v213, v77
	v_add_f32_e32 v213, v213, v78
	v_add_f32_e32 v213, v213, v79
	v_cvt_pk_bf16_f32 v72, v72, v73
	v_cvt_pk_bf16_f32 v73, v74, v75
	v_cvt_pk_bf16_f32 v74, v76, v77
	v_cvt_pk_bf16_f32 v75, v78, v79
	v_max3_f32 v214, v80, v96, v81
	v_max3_f32 v214, v214, v97, v82
	v_max3_f32 v214, v214, v98, v83
	v_max3_f32 v214, v214, v99, v84
	v_max3_f32 v214, v214, v100, v85
	v_max3_f32 v214, v214, v101, v86
	v_max3_f32 v214, v214, v102, v87
	v_max3_f32 v214, v214, v103, v88
	v_add_f32_e32 v212, v212, v213
	s_waitcnt lgkmcnt(3)
	v_mfma_f32_32x32x16_bf16 v[0:15], v[136:139], v[72:75], v[0:15]
	v_max3_f32 v214, v214, v104, v89
	v_max3_f32 v214, v214, v105, v90
	v_max3_f32 v214, v214, v106, v91
	v_max3_f32 v214, v214, v107, v92
	s_waitcnt lgkmcnt(2)
	v_mfma_f32_32x32x16_bf16 v[16:31], v[140:143], v[72:75], v[16:31]
	v_max3_f32 v214, v214, v108, v93
	v_max3_f32 v214, v214, v109, v94
	v_max3_f32 v214, v214, v110, v95
	v_max_f32_e32 v214, v214, v111
	v_mov_b32_e32 v218, v214
	s_nop 1
	v_permlane32_swap_b32_e32 v214, v218
	v_max_f32_e32 v214, v214, v218
	s_waitcnt lgkmcnt(0)
	s_barrier
	ds_read_b128 v[112:115], v216
	ds_read_b128 v[116:119], v216 offset:4608
	ds_read_b128 v[120:123], v216 offset:32
	ds_read_b128 v[124:127], v216 offset:4640
	ds_read2_b64 v[128:131], v200 offset1:2
	ds_read2_b64 v[132:135], v211 offset1:2
	ds_read2_b64 v[136:139], v200 offset0:4 offset1:6
	ds_read2_b64 v[140:143], v211 offset0:4 offset1:6
	s_cmp_lg_u32 s40, 0
	s_cbranch_scc1 .Lfa_resc3
	v_cmp_lt_f32_e32 vcc, 0x40c00000, v214
	s_cbranch_vccnz .Lfa_resc3
.Lfa_cont3:
	v_exp_f32_e32 v80, v80
	v_exp_f32_e32 v81, v81
	v_exp_f32_e32 v82, v82
	v_exp_f32_e32 v83, v83
	s_waitcnt lgkmcnt(7)
	v_mfma_f32_32x32x16_bf16 v[48:63], v[112:115], v[144:147], v[32:47]
	v_exp_f32_e32 v84, v84
	v_exp_f32_e32 v85, v85
	v_exp_f32_e32 v86, v86
	v_exp_f32_e32 v87, v87
	s_waitcnt lgkmcnt(6)
	v_mfma_f32_32x32x16_bf16 v[64:79], v[116:119], v[144:147], v[32:47]
	v_add_f32_e32 v213, v80, v81
	v_add_f32_e32 v213, v213, v82
	v_add_f32_e32 v213, v213, v83
	s_waitcnt lgkmcnt(5)
	v_mfma_f32_32x32x16_bf16 v[48:63], v[120:123], v[148:151], v[48:63]
	v_add_f32_e32 v213, v213, v84
	v_add_f32_e32 v213, v213, v85
	v_add_f32_e32 v213, v213, v86
	v_add_f32_e32 v213, v213, v87
	s_waitcnt lgkmcnt(4)
	v_mfma_f32_32x32x16_bf16 v[64:79], v[124:127], v[148:151], v[64:79]
	v_cvt_pk_bf16_f32 v80, v80, v81
	v_cvt_pk_bf16_f32 v81, v82, v83
	v_cvt_pk_bf16_f32 v82, v84, v85
	v_cvt_pk_bf16_f32 v83, v86, v87
	ds_read_b128 v[112:115], v216 offset:64
	ds_read_b128 v[116:119], v216 offset:4672
	ds_read_b128 v[120:123], v216 offset:96
	ds_read_b128 v[124:127], v216 offset:4704
	v_exp_f32_e32 v88, v88
	v_exp_f32_e32 v89, v89
	s_waitcnt lgkmcnt(7)
	v_mfma_f32_32x32x16_bf16 v[0:15], v[128:131], v[80:83], v[0:15]
	v_exp_f32_e32 v90, v90
	v_exp_f32_e32 v91, v91
	v_exp_f32_e32 v92, v92
	s_waitcnt lgkmcnt(6)
	v_mfma_f32_32x32x16_bf16 v[16:31], v[132:135], v[80:83], v[16:31]
	v_exp_f32_e32 v93, v93
	v_exp_f32_e32 v94, v94
	v_exp_f32_e32 v95, v95
	s_waitcnt lgkmcnt(3)
	v_mfma_f32_32x32x16_bf16 v[48:63], v[112:115], v[152:155], v[48:63]
	v_add_f32_e32 v213, v213, v88
	v_add_f32_e32 v213, v213, v89
	v_add_f32_e32 v213, v213, v90
	v_add_f32_e32 v213, v213, v91
	s_waitcnt lgkmcnt(2)
	v_mfma_f32_32x32x16_bf16 v[64:79], v[116:119], v[152:155], v[64:79]
	v_add_f32_e32 v213, v213, v92
	v_add_f32_e32 v213, v213, v93
	v_add_f32_e32 v213, v213, v94
	v_add_f32_e32 v213, v213, v95
	v_cvt_pk_bf16_f32 v88, v88, v89
	v_cvt_pk_bf16_f32 v89, v90, v91
	v_cvt_pk_bf16_f32 v90, v92, v93
	v_cvt_pk_bf16_f32 v91, v94, v95
	v_exp_f32_e32 v96, v96
	v_exp_f32_e32 v97, v97
	v_mfma_f32_32x32x16_bf16 v[0:15], v[136:139], v[88:91], v[0:15]
	v_exp_f32_e32 v98, v98
	v_exp_f32_e32 v99, v99
	v_exp_f32_e32 v100, v100
	v_mfma_f32_32x32x16_bf16 v[16:31], v[140:143], v[88:91], v[16:31]
	ds_read2_b64 v[128:131], v200 offset0:8 offset1:10
	ds_read2_b64 v[132:135], v211 offset0:8 offset1:10
	ds_read2_b64 v[136:139], v200 offset0:12 offset1:14
	ds_read2_b64 v[140:143], v211 offset0:12 offset1:14
	v_exp_f32_e32 v101, v101
	v_exp_f32_e32 v102, v102
	v_exp_f32_e32 v103, v103
	s_waitcnt lgkmcnt(5)
	v_mfma_f32_32x32x16_bf16 v[48:63], v[120:123], v[156:159], v[48:63]
	v_add_f32_e32 v213, v213, v96
	v_add_f32_e32 v213, v213, v97
	v_add_f32_e32 v213, v213, v98
	v_add_f32_e32 v213, v213, v99
	s_waitcnt lgkmcnt(4)
	v_mfma_f32_32x32x16_bf16 v[64:79], v[124:127], v[156:159], v[64:79]
	v_add_f32_e32 v213, v213, v100
	v_add_f32_e32 v213, v213, v101
	v_add_f32_e32 v213, v213, v102
	v_add_f32_e32 v213, v213, v103
	v_cvt_pk_bf16_f32 v96, v96, v97
	v_cvt_pk_bf16_f32 v97, v98, v99
	v_cvt_pk_bf16_f32 v98, v100, v101
	v_cvt_pk_bf16_f32 v99, v102, v103
	v_exp_f32_e32 v104, v104
	v_exp_f32_e32 v105, v105
	s_waitcnt lgkmcnt(3)
	v_mfma_f32_32x32x16_bf16 v[0:15], v[128:131], v[96:99], v[0:15]
	v_exp_f32_e32 v106, v106
	v_exp_f32_e32 v107, v107
	v_exp_f32_e32 v108, v108
	s_waitcnt lgkmcnt(2)
	v_mfma_f32_32x32x16_bf16 v[16:31], v[132:135], v[96:99], v[16:31]
	v_exp_f32_e32 v109, v109
	v_exp_f32_e32 v110, v110
	v_exp_f32_e32 v111, v111
	s_add_i32 s10, s29, 9
	s_min_i32 s10, s10, 0x43
	s_cmp_lt_i32 s10, 64
	s_cselect_b32 s11, s20, s41
	s_lshl_b32 s10, s10, 6
	s_add_i32 s10, s10, s11
	v_add_u32_e32 v112, s10, v197
	s_movk_i32 s10, 0x4a00
	v_mad_i64_i32 v[112:113], s[10:11], v112, s10, v[204:205]
	s_add_i32 s14, s29, 8
	s_min_i32 s14, s14, 0x43
	s_lshl_b32 s14, s14, 6
	s_mov_b32 s15, 0
	v_add_f32_e32 v213, v213, v104
	v_add_f32_e32 v213, v213, v105
	v_add_f32_e32 v213, v213, v106
	v_add_f32_e32 v213, v213, v107
	s_waitcnt vmcnt(7)
	ds_write_b128 v199, v[184:187] offset:17920
	s_waitcnt vmcnt(6)
	ds_write2_b64 v203, v[188:189], v[190:191] offset1:1
	v_lshl_add_u64 v[114:115], s[14:15], 1, v[206:207]
	global_load_dwordx4 v[184:187], v[112:113], off
	global_load_dwordx4 v[188:191], v[114:115], off
	v_add_f32_e32 v213, v213, v108
	v_add_f32_e32 v213, v213, v109
	v_add_f32_e32 v213, v213, v110
	v_add_f32_e32 v213, v213, v111
	v_cvt_pk_bf16_f32 v104, v104, v105
	v_cvt_pk_bf16_f32 v105, v106, v107
	v_cvt_pk_bf16_f32 v106, v108, v109
	v_cvt_pk_bf16_f32 v107, v110, v111
	v_max3_f32 v214, v48, v64, v49
	v_max3_f32 v214, v214, v65, v50
	v_max3_f32 v214, v214, v66, v51
	v_max3_f32 v214, v214, v67, v52
	v_max3_f32 v214, v214, v68, v53
	v_max3_f32 v214, v214, v69, v54
	v_max3_f32 v214, v214, v70, v55
	v_max3_f32 v214, v214, v71, v56
	v_add_f32_e32 v212, v212, v213
	s_waitcnt lgkmcnt(3)
	v_mfma_f32_32x32x16_bf16 v[0:15], v[136:139], v[104:107], v[0:15]
	v_max3_f32 v214, v214, v72, v57
	v_max3_f32 v214, v214, v73, v58
	v_max3_f32 v214, v214, v74, v59
	v_max3_f32 v214, v214, v75, v60
	s_waitcnt lgkmcnt(2)
	v_mfma_f32_32x32x16_bf16 v[16:31], v[140:143], v[104:107], v[16:31]
	v_max3_f32 v214, v214, v76, v61
	v_max3_f32 v214, v214, v77, v62
	v_max3_f32 v214, v214, v78, v63
	v_max_f32_e32 v214, v214, v79
	v_mov_b32_e32 v218, v214
	s_nop 1
	v_permlane32_swap_b32_e32 v214, v218
	v_max_f32_e32 v214, v214, v218
	s_waitcnt lgkmcnt(0)
	s_barrier
	s_add_i32 s29, s29, 4
	s_cmp_lt_i32 s29, 68
	s_cbranch_scc1 .Lfa_loop
	s_branch .LBB0_908
.Lfa_resc0:
	s_nop 7
	s_nop 7
	s_cmp_lg_u32 s40, 0
	s_cselect_b32 s10, 0xc2f00000, 0
	v_max_f32_e32 v214, s10, v214
	v_exp_f32_e64 v218, -v214
	v_add_f32_e32 v215, v215, v214
	v_xor_b32_e32 v32, 0x80000000, v215
	v_mul_f32_e32 v212, v212, v218
	v_mul_f32_e32 v0, v0, v218
	v_mul_f32_e32 v1, v1, v218
	v_mul_f32_e32 v2, v2, v218
	v_mul_f32_e32 v3, v3, v218
	v_mul_f32_e32 v4, v4, v218
	v_mul_f32_e32 v5, v5, v218
	v_mul_f32_e32 v6, v6, v218
	v_mul_f32_e32 v7, v7, v218
	v_mul_f32_e32 v8, v8, v218
	v_mul_f32_e32 v9, v9, v218
	v_mul_f32_e32 v10, v10, v218
	v_mul_f32_e32 v11, v11, v218
	v_mul_f32_e32 v12, v12, v218
	v_mul_f32_e32 v13, v13, v218
	v_mul_f32_e32 v14, v14, v218
	v_mul_f32_e32 v15, v15, v218
	v_mul_f32_e32 v16, v16, v218
	v_mul_f32_e32 v17, v17, v218
	v_mul_f32_e32 v18, v18, v218
	v_mul_f32_e32 v19, v19, v218
	v_mul_f32_e32 v20, v20, v218
	v_mul_f32_e32 v21, v21, v218
	v_mul_f32_e32 v22, v22, v218
	v_mul_f32_e32 v23, v23, v218
	v_mul_f32_e32 v24, v24, v218
	v_mul_f32_e32 v25, v25, v218
	v_mul_f32_e32 v26, v26, v218
	v_mul_f32_e32 v27, v27, v218
	v_mul_f32_e32 v28, v28, v218
	v_mul_f32_e32 v29, v29, v218
	v_mul_f32_e32 v30, v30, v218
	v_mul_f32_e32 v31, v31, v218
	v_sub_f32_e32 v48, v48, v214
	v_sub_f32_e32 v49, v49, v214
	v_sub_f32_e32 v50, v50, v214
	v_sub_f32_e32 v51, v51, v214
	v_sub_f32_e32 v52, v52, v214
	v_sub_f32_e32 v53, v53, v214
	v_sub_f32_e32 v54, v54, v214
	v_sub_f32_e32 v55, v55, v214
	v_sub_f32_e32 v56, v56, v214
	v_sub_f32_e32 v57, v57, v214
	v_sub_f32_e32 v58, v58, v214
	v_sub_f32_e32 v59, v59, v214
	v_sub_f32_e32 v60, v60, v214
	v_sub_f32_e32 v61, v61, v214
	v_sub_f32_e32 v62, v62, v214
	v_sub_f32_e32 v63, v63, v214
	v_sub_f32_e32 v64, v64, v214
	v_sub_f32_e32 v65, v65, v214
	v_sub_f32_e32 v66, v66, v214
	v_sub_f32_e32 v67, v67, v214
	v_sub_f32_e32 v68, v68, v214
	v_sub_f32_e32 v69, v69, v214
	v_sub_f32_e32 v70, v70, v214
	v_sub_f32_e32 v71, v71, v214
	v_sub_f32_e32 v72, v72, v214
	v_sub_f32_e32 v73, v73, v214
	v_sub_f32_e32 v74, v74, v214
	v_sub_f32_e32 v75, v75, v214
	v_sub_f32_e32 v76, v76, v214
	v_sub_f32_e32 v77, v77, v214
	v_sub_f32_e32 v78, v78, v214
	v_sub_f32_e32 v79, v79, v214
	v_mov_b32_e32 v33, v32
	v_mov_b32_e32 v34, v32
	v_mov_b32_e32 v35, v32
	v_mov_b32_e32 v36, v32
	v_mov_b32_e32 v37, v32
	v_mov_b32_e32 v38, v32
	v_mov_b32_e32 v39, v32
	v_mov_b32_e32 v40, v32
	v_mov_b32_e32 v41, v32
	v_mov_b32_e32 v42, v32
	v_mov_b32_e32 v43, v32
	v_mov_b32_e32 v44, v32
	v_mov_b32_e32 v45, v32
	v_mov_b32_e32 v46, v32
	v_mov_b32_e32 v47, v32
	s_mov_b32 s40, 0
	s_nop 1
	s_branch .Lfa_cont0
.Lfa_resc1:
	s_nop 7
	s_nop 7
	s_cmp_lg_u32 s40, 0
	s_cselect_b32 s10, 0xc2f00000, 0
	v_max_f32_e32 v214, s10, v214
	v_exp_f32_e64 v218, -v214
	v_add_f32_e32 v215, v215, v214
	v_xor_b32_e32 v32, 0x80000000, v215
	v_mul_f32_e32 v212, v212, v218
	v_mul_f32_e32 v0, v0, v218
	v_mul_f32_e32 v1, v1, v218
	v_mul_f32_e32 v2, v2, v218
	v_mul_f32_e32 v3, v3, v218
	v_mul_f32_e32 v4, v4, v218
	v_mul_f32_e32 v5, v5, v218
	v_mul_f32_e32 v6, v6, v218
	v_mul_f32_e32 v7, v7, v218
	v_mul_f32_e32 v8, v8, v218
	v_mul_f32_e32 v9, v9, v218
	v_mul_f32_e32 v10, v10, v218
	v_mul_f32_e32 v11, v11, v218
	v_mul_f32_e32 v12, v12, v218
	v_mul_f32_e32 v13, v13, v218
	v_mul_f32_e32 v14, v14, v218
	v_mul_f32_e32 v15, v15, v218
	v_mul_f32_e32 v16, v16, v218
	v_mul_f32_e32 v17, v17, v218
	v_mul_f32_e32 v18, v18, v218
	v_mul_f32_e32 v19, v19, v218
	v_mul_f32_e32 v20, v20, v218
	v_mul_f32_e32 v21, v21, v218
	v_mul_f32_e32 v22, v22, v218
	v_mul_f32_e32 v23, v23, v218
	v_mul_f32_e32 v24, v24, v218
	v_mul_f32_e32 v25, v25, v218
	v_mul_f32_e32 v26, v26, v218
	v_mul_f32_e32 v27, v27, v218
	v_mul_f32_e32 v28, v28, v218
	v_mul_f32_e32 v29, v29, v218
	v_mul_f32_e32 v30, v30, v218
	v_mul_f32_e32 v31, v31, v218
	v_sub_f32_e32 v80, v80, v214
	v_sub_f32_e32 v81, v81, v214
	v_sub_f32_e32 v82, v82, v214
	v_sub_f32_e32 v83, v83, v214
	v_sub_f32_e32 v84, v84, v214
	v_sub_f32_e32 v85, v85, v214
	v_sub_f32_e32 v86, v86, v214
	v_sub_f32_e32 v87, v87, v214
	v_sub_f32_e32 v88, v88, v214
	v_sub_f32_e32 v89, v89, v214
	v_sub_f32_e32 v90, v90, v214
	v_sub_f32_e32 v91, v91, v214
	v_sub_f32_e32 v92, v92, v214
	v_sub_f32_e32 v93, v93, v214
	v_sub_f32_e32 v94, v94, v214
	v_sub_f32_e32 v95, v95, v214
	v_sub_f32_e32 v96, v96, v214
	v_sub_f32_e32 v97, v97, v214
	v_sub_f32_e32 v98, v98, v214
	v_sub_f32_e32 v99, v99, v214
	v_sub_f32_e32 v100, v100, v214
	v_sub_f32_e32 v101, v101, v214
	v_sub_f32_e32 v102, v102, v214
	v_sub_f32_e32 v103, v103, v214
	v_sub_f32_e32 v104, v104, v214
	v_sub_f32_e32 v105, v105, v214
	v_sub_f32_e32 v106, v106, v214
	v_sub_f32_e32 v107, v107, v214
	v_sub_f32_e32 v108, v108, v214
	v_sub_f32_e32 v109, v109, v214
	v_sub_f32_e32 v110, v110, v214
	v_sub_f32_e32 v111, v111, v214
	v_mov_b32_e32 v33, v32
	v_mov_b32_e32 v34, v32
	v_mov_b32_e32 v35, v32
	v_mov_b32_e32 v36, v32
	v_mov_b32_e32 v37, v32
	v_mov_b32_e32 v38, v32
	v_mov_b32_e32 v39, v32
	v_mov_b32_e32 v40, v32
	v_mov_b32_e32 v41, v32
	v_mov_b32_e32 v42, v32
	v_mov_b32_e32 v43, v32
	v_mov_b32_e32 v44, v32
	v_mov_b32_e32 v45, v32
	v_mov_b32_e32 v46, v32
	v_mov_b32_e32 v47, v32
	s_mov_b32 s40, 0
	s_nop 1
	s_branch .Lfa_cont1
